# hand-written grid barrier (all workgroups poll the top-level release word, generations in SGPRs); U->V and V->LN2 seams synchronise only the four XCDs of a half (their data stays inside the half)
# baseline (speedup 1.0000x reference)
; __device__ __forceinline__ int mk_lane() { int l_ = (int)__builtin_amdgcn_mbcnt_hi(~0u, __builtin_amdgcn_mbcnt_lo(~0u, 0u)); asm volatile("" : "+v"(l_)); return l_; }
; __device__ __forceinline__ unsigned xb_ld(unsigned* p)              { return __hip_atomic_load(p, __ATOMIC_RELAXED, __HIP_MEMORY_SCOPE_AGENT); }
; __device__ __forceinline__ unsigned xb_add(unsigned* p, unsigned v) { return __hip_atomic_fetch_add(p, v, __ATOMIC_RELAXED, __HIP_MEMORY_SCOPE_AGENT); }
; #define XB_SPIN(cond, bar) do { unsigned _sp = 0; while (cond) { __builtin_amdgcn_s_sleep(1); \
;     if ((++_sp & 255u) == 0u) { if (xb_ld(&(bar)[XB_TMO])) break; if (_sp > XB_SPIN_CAP) { atomicAdd(&(bar)[XB_TMO], 1u); break; } } } } while (0)
; __device__ __forceinline__ void xcd_barrier(const XcdBarrier& b, int wave_id, int pair = -1) {
;     asm volatile("s_waitcnt vmcnt(0)" ::: "memory");
;     __syncthreads();
;     if (wave_id == 0 && mk_lane() == 0) {
;         unsigned* bar = b.bar;
;         __builtin_amdgcn_s_waitcnt(0);
;         unsigned nloc = b.st[0], nx = b.st[1];
;         if (nloc == 0u) { xcd_barrier_complete(bar, b.x, nloc, nx); b.st[0] = nloc; b.st[1] = nx; }
;         const unsigned old = xb_add(&bar[XB_XSUB(b.x)], 1u);
;         const unsigned gen = old / nloc;
;         if (old + 1u == (gen + 1u) * nloc) {
;             __builtin_amdgcn_fence(__ATOMIC_RELEASE, "agent");
;             asm volatile("s_waitcnt vmcnt(0)" ::: "memory");
;             unsigned* topw = pair < 0 ? &bar[XB_TOP] : &bar[XB_PTOP(pair)]; unsigned* topg = pair < 0 ? &bar[XB_TOPGEN] : &bar[XB_PTOPGEN(pair)];
;             if (pair >= 0) nx = 2u;
;             const unsigned og = xb_add(topw, 1u);
;             const unsigned tg = og / nx;
;             if (og + 1u == (tg + 1u) * nx) xb_add(topg, 1u);
;             else XB_SPIN(xb_ld(topg) == tg, bar);
;             __builtin_amdgcn_fence(__ATOMIC_ACQUIRE, "agent");
;             xb_add(&bar[XB_XGEN(b.x)], 1u);
;             asm volatile("s_waitcnt vmcnt(0)" ::: "memory");
.LBB0_72:
	s_waitcnt lgkmcnt(0)
	v_readfirstlane_b32 s16, v2
	v_readfirstlane_b32 s17, v0
	s_add_u32 s8, s30, 0x4000
	s_addc_u32 s9, s31, 0
	s_lshl_b32 s12, s33, 8
	s_add_u32 s10, s8, s12
	s_addc_u32 s11, s9, 0
	s_movk_i32 s24, 0x3400
	s_movk_i32 s25, 0x3500
	s_mov_b32 s21, s100
	s_mov_b32 s22, 0
	s_add_u32 s12, s8, s24
	s_addc_u32 s13, s9, 0
	s_add_u32 s14, s8, s25
	s_addc_u32 s15, s9, 0
	s_and_b32 s18, s101, 0xffff
	s_lshr_b32 s19, s101, 16
	s_add_i32 s18, s18, s19
	s_add_i32 s18, s18, s100
	s_add_i32 s18, s18, 1
	s_mul_i32 s18, s18, s16
	v_mov_b32_e32 v1, 0
	v_mov_b32_e32 v3, 0x1000
	v_mov_b32_e32 v4, 1
	global_atomic_add v3, v3, v4, s[10:11] offset:1024 sc0
	s_waitcnt vmcnt(0)
	v_readfirstlane_b32 s19, v3
	s_add_i32 s19, s19, 1
	s_cmp_lg_u32 s19, s18
	s_cbranch_scc1 .Lxb0_nonleader
	buffer_wbl2 sc1
	buffer_inv sc1
	s_add_i32 s18, s21, 1
	s_mul_i32 s18, s18, s17
	s_waitcnt vmcnt(0)
	global_atomic_add v3, v1, v4, s[12:13] sc0
	s_waitcnt vmcnt(0)
	v_readfirstlane_b32 s19, v3
	s_add_i32 s19, s19, 1
	s_cmp_lg_u32 s19, s18
	s_cbranch_scc1 .Lxb0_spin
	global_atomic_add v1, v4, s[14:15]
	s_branch .Lxb0_done

; __device__ __forceinline__ unsigned xb_ld(unsigned* p)              { return __hip_atomic_load(p, __ATOMIC_RELAXED, __HIP_MEMORY_SCOPE_AGENT); }
; __device__ __forceinline__ unsigned xb_add(unsigned* p, unsigned v) { return __hip_atomic_fetch_add(p, v, __ATOMIC_RELAXED, __HIP_MEMORY_SCOPE_AGENT); }
; #define XB_SPIN(cond, bar) do { unsigned _sp = 0; while (cond) { __builtin_amdgcn_s_sleep(1); \
;     if ((++_sp & 255u) == 0u) { if (xb_ld(&(bar)[XB_TMO])) break; if (_sp > XB_SPIN_CAP) { atomicAdd(&(bar)[XB_TMO], 1u); break; } } } } while (0)
; __device__ __forceinline__ void xcd_barrier(const XcdBarrier& b, int wave_id, int pair = -1) {
;     ...
;         const unsigned old = xb_add(&bar[XB_XSUB(b.x)], 1u);
;         const unsigned gen = old / nloc;
;         if (old + 1u == (gen + 1u) * nloc) {
;             __builtin_amdgcn_fence(__ATOMIC_RELEASE, "agent");
;             asm volatile("s_waitcnt vmcnt(0)" ::: "memory");
;             unsigned* topw = pair < 0 ? &bar[XB_TOP] : &bar[XB_PTOP(pair)]; unsigned* topg = pair < 0 ? &bar[XB_TOPGEN] : &bar[XB_PTOPGEN(pair)];
;             if (pair >= 0) nx = 2u;
;             const unsigned og = xb_add(topw, 1u);
;             const unsigned tg = og / nx;
;             if (og + 1u == (tg + 1u) * nx) xb_add(topg, 1u);
;             else XB_SPIN(xb_ld(topg) == tg, bar);
;             __builtin_amdgcn_fence(__ATOMIC_ACQUIRE, "agent");
;             xb_add(&bar[XB_XGEN(b.x)], 1u);
;             asm volatile("s_waitcnt vmcnt(0)" ::: "memory");
;         } else {
;             XB_SPIN(xb_ld(&bar[XB_XGEN(b.x)]) == gen, bar);
;             __builtin_amdgcn_fence(__ATOMIC_ACQUIRE, "agent");
;             asm volatile("s_waitcnt vmcnt(0)" ::: "memory");
;         }
.Lxb0_done:
	s_add_i32 s101, s101, s22
	s_cmp_eq_u32 s22, 0
	s_cselect_b32 s22, 1, 0
	s_add_i32 s100, s100, s22
	s_waitcnt vmcnt(0)

; __device__ __forceinline__ int mk_lane() { int l_ = (int)__builtin_amdgcn_mbcnt_hi(~0u, __builtin_amdgcn_mbcnt_lo(~0u, 0u)); asm volatile("" : "+v"(l_)); return l_; }
; __device__ __forceinline__ unsigned xb_ld(unsigned* p)              { return __hip_atomic_load(p, __ATOMIC_RELAXED, __HIP_MEMORY_SCOPE_AGENT); }
; __device__ __forceinline__ void xcd_barrier(const XcdBarrier& b, int wave_id, int pair = -1) {
;     asm volatile("s_waitcnt vmcnt(0)" ::: "memory");
;     __syncthreads();
;     if (wave_id == 0 && mk_lane() == 0) {
;         unsigned* bar = b.bar;
;         __builtin_amdgcn_s_waitcnt(0);
;         unsigned nloc = b.st[0], nx = b.st[1];
;         if (nloc == 0u) { xcd_barrier_complete(bar, b.x, nloc, nx); b.st[0] = nloc; b.st[1] = nx; }
;         const unsigned old = xb_add(&bar[XB_XSUB(b.x)], 1u);
;         const unsigned gen = old / nloc;
;         if (old + 1u == (gen + 1u) * nloc) {
;             __builtin_amdgcn_fence(__ATOMIC_RELEASE, "agent");
;             asm volatile("s_waitcnt vmcnt(0)" ::: "memory");
;             unsigned* topw = pair < 0 ? &bar[XB_TOP] : &bar[XB_PTOP(pair)]; unsigned* topg = pair < 0 ? &bar[XB_TOPGEN] : &bar[XB_PTOPGEN(pair)];
;             if (pair >= 0) nx = 2u;
;             const unsigned og = xb_add(topw, 1u);
;             const unsigned tg = og / nx;
;             if (og + 1u == (tg + 1u) * nx) xb_add(topg, 1u);
;             else XB_SPIN(xb_ld(topg) == tg, bar);
;             __builtin_amdgcn_fence(__ATOMIC_ACQUIRE, "agent");
;             xb_add(&bar[XB_XGEN(b.x)], 1u);
;             asm volatile("s_waitcnt vmcnt(0)" ::: "memory");
; template <int K> __device__ __forceinline__ void run_phase(Frame& F, const XcdBarrier& bar, int lo, int hi, unsigned char* lds) {
;     ...
;             constexpr bool PAIR_SEAM = MK_LOCALBAR && (sub == 0 || sub == 1);
;             bool pairok = false;
;             if (PAIR_SEAM) pairok = __hip_atomic_load((unsigned*)(F.ctl + CW_LBAR + 24 * 64), __ATOMIC_RELAXED, __HIP_MEMORY_SCOPE_AGENT) == 0u;
;             if (local) xcd_local_barrier((unsigned*)(F.ctl + CW_LBAR + ((sub == 2 ? l : 2) * 8 + (bx & 7)) * 64), (unsigned)(G >> 3), (unsigned*)(F.ctl + CW_BAR) + XB_TMO, F.wave);
;             else xcd_barrier(bar, F.wave, pairok ? ((bx & 7) >> 1) : -1);
.LBB0_209:
	s_waitcnt lgkmcnt(0)
	v_readfirstlane_b32 s16, v3
	v_readfirstlane_b32 s17, v1
	s_add_u32 s8, s30, 0x4000
	s_addc_u32 s9, s31, 0
	s_lshl_b32 s12, s33, 8
	s_add_u32 s10, s8, s12
	s_addc_u32 s11, s9, 0
	s_movk_i32 s24, 0x3400
	s_movk_i32 s25, 0x3500
	s_mov_b32 s21, s100
	s_mov_b32 s22, 0
	v_readfirstlane_b32 s23, v0
	s_cmp_lg_u32 s23, 0
	s_cbranch_scc1 .Lxb1_full
	s_lshl_b32 s23, s2, 7
	s_and_b32 s23, s23, 0x300
	s_add_i32 s24, s23, 0x3600
	s_add_i32 s25, s23, 0x3a00
	s_mov_b32 s17, 2
	s_and_b32 s21, s101, 0xffff
	s_mov_b32 s22, 1
.Lxb1_full:
	s_add_u32 s12, s8, s24
	s_addc_u32 s13, s9, 0
	s_add_u32 s14, s8, s25
	s_addc_u32 s15, s9, 0
	s_and_b32 s18, s101, 0xffff
	s_lshr_b32 s19, s101, 16
	s_add_i32 s18, s18, s19
	s_add_i32 s18, s18, s100
	s_add_i32 s18, s18, 1
	s_mul_i32 s18, s18, s16
	v_mov_b32_e32 v2, 0
	v_mov_b32_e32 v4, 0x1000
	v_mov_b32_e32 v5, 1
	global_atomic_add v4, v4, v5, s[10:11] offset:1024 sc0
	s_waitcnt vmcnt(0)
	v_readfirstlane_b32 s19, v4
	s_add_i32 s19, s19, 1
	s_cmp_lg_u32 s19, s18
	s_cbranch_scc1 .Lxb1_nonleader
	buffer_wbl2 sc1
	buffer_inv sc1
	s_add_i32 s18, s21, 1
	s_mul_i32 s18, s18, s17
	s_waitcnt vmcnt(0)
	global_atomic_add v4, v2, v5, s[12:13] sc0
	s_waitcnt vmcnt(0)
	v_readfirstlane_b32 s19, v4
	s_add_i32 s19, s19, 1
	s_cmp_lg_u32 s19, s18
	s_cbranch_scc1 .Lxb1_spin
	global_atomic_add v2, v5, s[14:15]
	s_branch .Lxb1_done

; __device__ __forceinline__ unsigned xb_ld(unsigned* p)              { return __hip_atomic_load(p, __ATOMIC_RELAXED, __HIP_MEMORY_SCOPE_AGENT); }
; __device__ __forceinline__ void xcd_barrier(const XcdBarrier& b, int wave_id, int pair = -1) {
;     asm volatile("s_waitcnt vmcnt(0)" ::: "memory");
;     __syncthreads();
;     if (wave_id == 0 && mk_lane() == 0) {
;         unsigned* bar = b.bar;
;         __builtin_amdgcn_s_waitcnt(0);
;         unsigned nloc = b.st[0], nx = b.st[1];
;         if (nloc == 0u) { xcd_barrier_complete(bar, b.x, nloc, nx); b.st[0] = nloc; b.st[1] = nx; }
;         const unsigned old = xb_add(&bar[XB_XSUB(b.x)], 1u);
;         const unsigned gen = old / nloc;
;         if (old + 1u == (gen + 1u) * nloc) {
;             __builtin_amdgcn_fence(__ATOMIC_RELEASE, "agent");
;             asm volatile("s_waitcnt vmcnt(0)" ::: "memory");
;             unsigned* topw = pair < 0 ? &bar[XB_TOP] : &bar[XB_PTOP(pair)]; unsigned* topg = pair < 0 ? &bar[XB_TOPGEN] : &bar[XB_PTOPGEN(pair)];
;             if (pair >= 0) nx = 2u;
;             const unsigned og = xb_add(topw, 1u);
;             const unsigned tg = og / nx;
;             if (og + 1u == (tg + 1u) * nx) xb_add(topg, 1u);
;             else XB_SPIN(xb_ld(topg) == tg, bar);
;             __builtin_amdgcn_fence(__ATOMIC_ACQUIRE, "agent");
;             xb_add(&bar[XB_XGEN(b.x)], 1u);
;             asm volatile("s_waitcnt vmcnt(0)" ::: "memory");
; template <int K> __device__ __forceinline__ void run_phase(Frame& F, const XcdBarrier& bar, int lo, int hi, unsigned char* lds) {
;     ...
;         if (BOTH(k)) {
;             constexpr bool LOCAL_SEAM = MK_LOCALBAR && (sub == 2 || (sub == 6 && l == 0));
;             bool local = false;
;             if (LOCAL_SEAM) local = __hip_atomic_load((unsigned*)(F.ctl + CW_LBAR + 24 * 64), __ATOMIC_RELAXED, __HIP_MEMORY_SCOPE_AGENT) == 0u;
;             constexpr bool PAIR_SEAM = MK_LOCALBAR && (sub == 0 || sub == 1);
;             bool pairok = false;
;             if (PAIR_SEAM) pairok = __hip_atomic_load((unsigned*)(F.ctl + CW_LBAR + 24 * 64), __ATOMIC_RELAXED, __HIP_MEMORY_SCOPE_AGENT) == 0u;
;             if (local) xcd_local_barrier((unsigned*)(F.ctl + CW_LBAR + ((sub == 2 ? l : 2) * 8 + (bx & 7)) * 64), (unsigned)(G >> 3), (unsigned*)(F.ctl + CW_BAR) + XB_TMO, F.wave);
;             else xcd_barrier(bar, F.wave, pairok ? ((bx & 7) >> 1) : -1);
.LBB0_913:
	s_waitcnt lgkmcnt(0)
	v_readfirstlane_b32 s16, v2
	v_readfirstlane_b32 s17, v0
	s_add_u32 s8, s30, 0x4000
	s_addc_u32 s9, s31, 0
	s_lshl_b32 s12, s33, 8
	s_add_u32 s10, s8, s12
	s_addc_u32 s11, s9, 0
	s_movk_i32 s24, 0x3400
	s_movk_i32 s25, 0x3500
	s_mov_b32 s21, s100
	s_mov_b32 s22, 0
	v_mov_b32_e32 v5, 0x31000
	global_load_dword v5, v5, s[30:31] offset:2048 sc1
	s_and_b32 s18, s101, 0xffff
	s_lshr_b32 s19, s101, 16
	s_add_i32 s18, s18, s19
	s_add_i32 s18, s18, s100
	s_add_i32 s18, s18, 1
	s_mul_i32 s18, s18, s16
	v_mov_b32_e32 v1, 0
	v_mov_b32_e32 v3, 0x1000
	v_mov_b32_e32 v4, 1
	global_atomic_add v3, v3, v4, s[10:11] offset:1024 sc0
	s_waitcnt vmcnt(0)
	v_readfirstlane_b32 s23, v5
	s_cmp_lg_u32 s23, 0
	s_cbranch_scc1 .Lxb5_full
	s_lshl_b32 s23, s2, 6
	s_and_b32 s23, s23, 0x100
	s_add_i32 s24, s23, 0x4000
	s_add_i32 s25, s23, 0x4400
	s_mov_b32 s17, 4
	s_lshr_b32 s21, s101, 16
	s_mov_b32 s22, 0x10000
.Lxb5_full:
	s_add_u32 s12, s8, s24
	s_addc_u32 s13, s9, 0
	s_add_u32 s14, s8, s25
	s_addc_u32 s15, s9, 0
	v_readfirstlane_b32 s19, v3
	s_add_i32 s19, s19, 1
	s_cmp_lg_u32 s19, s18
	s_cbranch_scc1 .Lxb5_nonleader
	buffer_wbl2 sc1
	buffer_inv sc1
	s_add_i32 s18, s21, 1
	s_mul_i32 s18, s18, s17
	s_waitcnt vmcnt(0)
	global_atomic_add v3, v1, v4, s[12:13] sc0
	s_waitcnt vmcnt(0)
	v_readfirstlane_b32 s19, v3
	s_add_i32 s19, s19, 1
	s_cmp_lg_u32 s19, s18
	s_cbranch_scc1 .Lxb5_spin
	global_atomic_add v1, v4, s[14:15]
	s_branch .Lxb5_done
